# ssm_final: coefficient, output-matrix, skip-gain and input loads hoisted to the unit top (one latency round instead of three)
# baseline (speedup 1.0000x reference)
.LBB0_519:
	v_ashrrev_i32_e32 v0, 31, v90
	v_lshrrev_b32_e32 v0, 27, v0
	v_add_u32_e32 v0, v90, v0
	v_ashrrev_i32_e32 v84, 5, v0
	v_mul_hi_i32 v0, v84, s78
	v_add_u32_e32 v0, v0, v84
	v_lshrrev_b32_e32 v1, 31, v0
	v_ashrrev_i32_e32 v0, 4, v0
	v_add_u32_e32 v0, v0, v1
	v_mov_b32_e32 v207, v0
	v_mul_lo_u32 v0, v0, 28
	v_sub_u32_e32 v0, v84, v0
	v_ashrrev_i32_e32 v1, 31, v0
	v_lshl_add_u64 v[2:3], v[0:1], 2, s[16:17]
	global_load_dword v1, v[2:3], off
	v_lshl_or_b32 v2, v0, 6, v91
	v_ashrrev_i32_e32 v3, 31, v2
	v_lshlrev_b64 v[4:5], 2, v[2:3]
	v_lshl_add_u64 v[6:7], s[14:15], 0, v[4:5]
	global_load_dword v77, v[6:7], off
	v_lshl_add_u64 v[4:5], s[12:13], 0, v[4:5]
	global_load_dword v76, v[4:5], off
	v_lshlrev_b64 v[132:133], 6, v[2:3]
	v_lshl_add_u64 v[134:135], s[20:21], 0, v[132:133]
	v_lshl_add_u64 v[132:133], s[18:19], 0, v[132:133]
	global_load_dwordx4 v[180:183], v[132:133], off
	global_load_dwordx4 v[184:187], v[134:135], off
	global_load_dwordx4 v[188:191], v[132:133], off offset:16
	global_load_dwordx4 v[192:195], v[134:135], off offset:16
	global_load_dwordx4 v[196:199], v[132:133], off offset:32
	global_load_dwordx4 v[200:203], v[134:135], off offset:32
	global_load_dwordx4 v[208:211], v[132:133], off offset:48
	global_load_dwordx4 v[212:215], v[134:135], off offset:48
	v_lshl_or_b32 v132, v0, 4, v92
	v_mov_b32_e32 v133, 0
	v_lshlrev_b64 v[134:135], 8, v[132:133]
	v_lshl_add_u64 v[134:135], v[134:135], 0, v[64:65]
	global_load_dwordx4 v[224:227], v[134:135], off
	global_load_dwordx4 v[228:231], v[134:135], off offset:16
	global_load_dwordx4 v[232:235], v[134:135], off offset:32
	global_load_dwordx4 v[236:239], v[134:135], off offset:48
	global_load_dwordx4 v[240:243], v[134:135], off offset:64
	global_load_dwordx4 v[244:247], v[134:135], off offset:80
	global_load_dwordx4 v[248:251], v[134:135], off offset:96
	global_load_dwordx4 v[216:219], v[134:135], off offset:112
	v_lshl_add_u64 v[134:135], v[132:133], 2, s[22:23]
	global_load_dword v206, v[134:135], off
	v_lshlrev_b32_e32 v132, 5, v84
	v_sub_u32_e32 v132, v90, v132
	v_mov_b64_e32 v[134:135], s[10:11]
	s_mov_b32 s4, 0x1060000
	s_mov_b32 s5, 0x83000
	v_mad_i64_i32 v[134:135], s[6:7], v207, s4, v[134:135]
	v_mad_i64_i32 v[134:135], s[6:7], v132, s5, v[134:135]
	v_lshlrev_b32_e32 v132, 5, v0
	v_lshl_add_u64 v[134:135], v[132:133], 0, v[134:135]
	v_mov_b32_e32 v132, v70
	v_lshl_add_u64 v[134:135], v[132:133], 0, v[134:135]
	global_load_dwordx4 v[136:139], v[134:135], off offset:2688
	global_load_dwordx4 v[140:143], v[134:135], off offset:2704
	s_waitcnt vmcnt(19) lgkmcnt(0)
	v_mul_f32_e32 v3, 0x3fb8aa3b, v1
	v_fma_f32 v4, v1, s81, -v3
	v_rndne_f32_e32 v5, v3
	v_fmac_f32_e32 v4, 0x32a5705f, v1
	v_sub_f32_e32 v3, v3, v5
	v_add_f32_e32 v3, v3, v4
	v_cvt_i32_f32_e32 v5, v5
	v_exp_f32_e32 v3, v3
	v_cmp_ngt_f32_e32 vcc, s86, v1
	v_ldexp_f32 v3, v3, v5
	s_nop 0
	v_cndmask_b32_e32 v3, 0, v3, vcc
	v_cmp_nlt_f32_e32 vcc, s92, v1
	s_nop 1
	v_cndmask_b32_e32 v4, v221, v3, vcc
	v_mul_f32_e32 v1, v77, v4
	v_and_b32_e32 v3, 0x7fffffff, v1
	v_lshrrev_b32_e32 v5, 23, v3
	v_and_b32_e32 v6, 0x7fffff, v3
	v_cmp_nlt_f32_e64 s[28:29], |v1|, s87
	v_add_u32_e32 v8, 0xffffff88, v5
	v_or_b32_e32 v7, 0x800000, v6
	s_and_saveexec_b64 s[0:1], s[28:29]
	s_xor_b64 s[30:31], exec, s[0:1]
	s_cbranch_execz .LBB0_521
	v_mad_u64_u32 v[10:11], s[6:7], v7, s88, 0
	v_mov_b32_e32 v144, v11
	v_mad_u64_u32 v[12:13], s[6:7], v7, s89, v[144:145]
	v_mov_b32_e32 v144, v13
	v_mad_u64_u32 v[14:15], s[6:7], v7, s90, v[144:145]
	v_cmp_lt_u32_e32 vcc, 63, v8
	v_mov_b32_e32 v144, v15
	v_mad_u64_u32 v[16:17], s[6:7], v7, s91, v[144:145]
	v_cndmask_b32_e32 v5, 0, v223, vcc
	v_add_u32_e32 v5, v5, v8
	v_mov_b32_e32 v144, v17
	s_mov_b32 s2, 0xfc2757d1
	v_cmp_lt_u32_e64 s[0:1], 31, v5
	v_not_b32_e32 v9, 31
	v_mad_u64_u32 v[18:19], s[6:7], v7, s2, v[144:145]
	v_cndmask_b32_e64 v6, 0, v9, s[0:1]
	v_mov_b32_e32 v144, v19
	s_mov_b32 s2, 0x4e441529
	v_add_u32_e32 v5, v6, v5
	v_mad_u64_u32 v[20:21], s[6:7], v7, s2, v[144:145]
	v_cmp_lt_u32_e64 s[4:5], 31, v5
	v_mov_b32_e32 v144, v21
	s_mov_b32 s2, 0xa2f9836e
	v_cndmask_b32_e64 v6, 0, v9, s[4:5]
	v_mad_u64_u32 v[22:23], s[6:7], v7, s2, v[144:145]
	v_add_u32_e32 v5, v6, v5
	v_cndmask_b32_e32 v6, v20, v16, vcc
	v_cndmask_b32_e32 v9, v22, v18, vcc
	v_cndmask_b32_e32 v13, v23, v20, vcc
	v_cndmask_b32_e64 v11, v9, v6, s[0:1]
	v_cndmask_b32_e64 v9, v13, v9, s[0:1]
	v_cndmask_b32_e32 v13, v18, v14, vcc
	v_cndmask_b32_e64 v6, v6, v13, s[0:1]
	v_cndmask_b32_e64 v9, v9, v11, s[4:5]
	v_cndmask_b32_e64 v11, v11, v6, s[4:5]
	v_sub_u32_e32 v15, 32, v5
	v_alignbit_b32 v17, v9, v11, v15
	v_cmp_eq_u32_e64 s[6:7], 0, v5
	v_cndmask_b32_e32 v10, v14, v10, vcc
	s_nop 0
	v_cndmask_b32_e64 v5, v17, v9, s[6:7]
	v_cndmask_b32_e32 v9, v16, v12, vcc
	v_cndmask_b32_e64 v12, v13, v9, s[0:1]
	v_cndmask_b32_e64 v6, v6, v12, s[4:5]
	v_alignbit_b32 v13, v11, v6, v15
	v_cndmask_b32_e64 v9, v9, v10, s[0:1]
	v_cndmask_b32_e64 v11, v13, v11, s[6:7]
	v_bfe_u32 v17, v5, 29, 1
	v_cndmask_b32_e64 v9, v12, v9, s[4:5]
	v_alignbit_b32 v13, v5, v11, 30
	v_sub_u32_e32 v18, 0, v17
	v_alignbit_b32 v10, v6, v9, v15
	v_xor_b32_e32 v13, v13, v18
	v_cndmask_b32_e64 v6, v10, v6, s[6:7]
	v_alignbit_b32 v10, v11, v6, 30
	v_ffbh_u32_e32 v11, v13
	v_min_u32_e32 v11, 32, v11
	v_alignbit_b32 v6, v6, v9, 30
	v_xor_b32_e32 v10, v10, v18
	v_sub_u32_e32 v12, 31, v11
	v_xor_b32_e32 v6, v6, v18
	v_alignbit_b32 v13, v13, v10, v12
	v_alignbit_b32 v6, v10, v6, v12
	v_alignbit_b32 v9, v13, v6, 9
	v_ffbh_u32_e32 v10, v9
	v_min_u32_e32 v10, 32, v10
	v_lshrrev_b32_e32 v16, 29, v5
	v_not_b32_e32 v12, v10
	v_alignbit_b32 v6, v9, v6, v12
	v_lshlrev_b32_e32 v9, 31, v16
	v_or_b32_e32 v12, 0x33000000, v9
	v_add_lshl_u32 v10, v10, v11, 23
	v_lshrrev_b32_e32 v6, 9, v6
	v_sub_u32_e32 v10, v12, v10
	v_or_b32_e32 v9, 0.5, v9
	v_lshlrev_b32_e32 v11, 23, v11
	v_or_b32_e32 v6, v10, v6
	v_lshrrev_b32_e32 v10, 9, v13
	v_sub_u32_e32 v9, v9, v11
	v_or_b32_e32 v9, v10, v9
	v_mul_f32_e32 v10, 0x3fc90fda, v9
	s_mov_b32 s0, 0x3fc90fda
	v_fma_f32 v11, v9, s0, -v10
	v_fmac_f32_e32 v11, 0x33a22168, v9
	v_fmac_f32_e32 v11, 0x3fc90fda, v6
	v_lshrrev_b32_e32 v5, 30, v5
	v_add_f32_e32 v6, v10, v11
	v_add_u32_e32 v5, v17, v5

.LBB0_527:
	s_or_b64 exec, exec, s[0:1]
	v_mul_f32_e32 v4, v76, v4
	v_mul_f32_e32 v7, 0x3fb8aa3b, v4
	v_fma_f32 v8, v4, s81, -v7
	v_rndne_f32_e32 v11, v7
	v_fmac_f32_e32 v8, 0x32a5705f, v4
	v_sub_f32_e32 v7, v7, v11
	v_add_f32_e32 v7, v7, v8
	v_exp_f32_e32 v7, v7
	v_cvt_i32_f32_e32 v8, v11
	v_cmp_ngt_f32_e32 vcc, s86, v4
	s_brev_b32 s0, 1
	v_lshlrev_b32_e32 v80, 4, v0
	v_ldexp_f32 v7, v7, v8
	v_cndmask_b32_e32 v7, 0, v7, vcc
	v_cmp_nlt_f32_e32 vcc, s92, v4
	v_lshlrev_b32_e32 v2, 4, v2
	v_or_b32_e32 v78, v80, v92
	v_cndmask_b32_e32 v4, v221, v7, vcc
	v_mul_f32_e32 v7, v6, v6
	v_fmamk_f32 v8, v7, 0xb94c1982, v253
	v_fmaak_f32 v8, v7, v8, 0xbe2aaa9d
	v_mul_f32_e32 v8, v7, v8
	v_fmac_f32_e32 v6, v6, v8
	v_fmamk_f32 v8, v7, 0x37d75334, v222
	v_fmaak_f32 v8, v7, v8, 0x3d2aabf7
	v_fmaak_f32 v8, v7, v8, 0xbf000004
	v_fma_f32 v7, v7, v8, 1.0
	v_and_b32_e32 v8, 1, v5
	v_cmp_eq_u32_e32 vcc, 0, v8
	v_lshlrev_b32_e32 v5, 30, v5
	v_ashrrev_i32_e32 v79, 31, v78
	v_cndmask_b32_e64 v6, -v6, v7, vcc
	v_bitop3_b32 v5, v5, v6, s0 bitop3:0x6c
	s_movk_i32 s0, 0x1f8
	v_cmp_class_f32_e64 vcc, v1, s0
	v_mov_b32_e32 v7, 0x7fc00000
	v_xor_b32_e32 v1, v3, v1
	v_cndmask_b32_e32 v5, v7, v5, vcc
	v_mul_f32_e32 v72, v4, v5
	v_lshlrev_b32_e32 v5, 5, v84
	v_sub_u32_e32 v82, v90, v5
	v_mul_f32_e32 v5, v10, v10
	v_fmamk_f32 v6, v5, 0xb94c1982, v253
	v_fmaak_f32 v6, v5, v6, 0xbe2aaa9d
	v_mul_f32_e32 v6, v5, v6
	v_fmac_f32_e32 v10, v10, v6
	v_fmamk_f32 v6, v5, 0x37d75334, v222
	v_fmaak_f32 v6, v5, v6, 0x3d2aabf7
	v_fmaak_f32 v6, v5, v6, 0xbf000004
	v_fma_f32 v5, v5, v6, 1.0
	v_and_b32_e32 v6, 1, v9
	v_cmp_eq_u32_e64 s[0:1], 0, v6
	v_lshlrev_b32_e32 v6, 30, v9
	v_and_b32_e32 v6, 0x80000000, v6
	v_cndmask_b32_e64 v5, v5, v10, s[0:1]
	v_xor_b32_e32 v1, v1, v6
	v_xor_b32_e32 v1, v1, v5
	v_cndmask_b32_e32 v1, v7, v1, vcc
	v_ashrrev_i32_e32 v3, 31, v2
	v_mul_f32_e32 v74, v4, v1
	v_lshlrev_b64 v[2:3], 2, v[2:3]
	v_lshlrev_b64 v[0:1], 8, v[78:79]
	v_lshl_add_u64 v[4:5], s[18:19], 0, v[2:3]
	v_lshl_add_u64 v[2:3], s[20:21], 0, v[2:3]
	v_lshl_add_u64 v[0:1], v[64:65], 0, v[0:1]
	s_waitcnt vmcnt(2)
	v_mov_b64_e32 v[56:57], v[180:181]
	v_mov_b64_e32 v[58:59], v[182:183]
	v_mov_b64_e32 v[60:61], v[184:185]
	v_mov_b64_e32 v[62:63], v[186:187]
	v_mov_b64_e32 v[48:49], v[188:189]
	v_mov_b64_e32 v[50:51], v[190:191]
	v_mov_b64_e32 v[52:53], v[192:193]
	v_mov_b64_e32 v[54:55], v[194:195]
	v_mov_b64_e32 v[40:41], v[196:197]
	v_mov_b64_e32 v[42:43], v[198:199]
	v_mov_b64_e32 v[44:45], v[200:201]
	v_mov_b64_e32 v[46:47], v[202:203]
	v_mov_b64_e32 v[24:25], v[208:209]
	v_mov_b64_e32 v[26:27], v[210:211]
	v_mov_b64_e32 v[36:37], v[212:213]
	v_mov_b64_e32 v[38:39], v[214:215]
	v_mov_b64_e32 v[32:33], v[224:225]
	v_mov_b64_e32 v[34:35], v[226:227]
	v_mov_b64_e32 v[28:29], v[228:229]
	v_mov_b64_e32 v[30:31], v[230:231]
	v_mov_b64_e32 v[20:21], v[232:233]
	v_mov_b64_e32 v[22:23], v[234:235]
	v_mov_b64_e32 v[16:17], v[236:237]
	v_mov_b64_e32 v[18:19], v[238:239]
	v_mov_b64_e32 v[12:13], v[240:241]
	v_mov_b64_e32 v[14:15], v[242:243]
	v_mov_b64_e32 v[8:9], v[244:245]
	v_mov_b64_e32 v[10:11], v[246:247]
	v_mov_b64_e32 v[4:5], v[248:249]
	v_mov_b64_e32 v[6:7], v[250:251]
	s_nop 0
	v_mov_b64_e32 v[0:1], v[216:217]
	v_mov_b64_e32 v[2:3], v[218:219]
	v_lshl_add_u64 v[78:79], v[78:79], 2, s[22:23]
	v_mov_b32_e32 v100, v206
	v_mov_b32_e32 v144, v145
	v_cmp_lt_i32_e32 vcc, 0, v82
	v_mov_b64_e32 v[78:79], v[144:145]
	s_and_saveexec_b64 s[0:1], vcc
	s_cbranch_execz .LBB0_531
	v_add_f32_e32 v73, v72, v72
	v_mul_f32_e32 v71, v74, v74
	v_mul_f32_e32 v73, v73, v74
	v_fma_f32 v71, v72, v72, -v71
	v_mul_f32_e32 v75, v73, v73
	v_fma_f32 v75, v71, v71, -v75
	v_add_f32_e32 v71, v71, v71
	v_mul_f32_e32 v71, v73, v71
	v_mul_f32_e32 v73, v71, v71
	v_fma_f32 v73, v75, v75, -v73
	v_add_f32_e32 v75, v75, v75
	v_mul_f32_e32 v71, v71, v75
	v_mul_f32_e32 v75, v71, v71
	v_fma_f32 v75, v73, v73, -v75
	v_add_f32_e32 v73, v73, v73
	v_mul_f32_e32 v71, v71, v73
	v_mul_f32_e32 v73, v71, v71
	v_fma_f32 v73, v75, v75, -v73
	v_add_f32_e32 v75, v75, v75
	v_mul_f32_e32 v71, v71, v75
	v_mul_f32_e32 v75, v71, v71
	v_ashrrev_i32_e32 v85, 31, v84
	v_fma_f32 v86, v73, v73, -v75
	v_add_f32_e32 v73, v73, v73
	v_lshlrev_b64 v[78:79], 14, v[84:85]
	v_mul_f32_e32 v88, v71, v73
	v_lshl_add_u64 v[84:85], s[24:25], 0, v[78:79]
	v_mov_b32_e32 v78, 0
	v_mov_b32_e32 v87, v86
	v_mov_b32_e32 v89, v88
	s_mov_b64 s[4:5], 0
	v_mov_b32_e32 v144, v91
	v_mov_b32_e32 v71, v82
	v_mov_b32_e32 v79, v78
	v_readfirstlane_b32 s6, v71
	s_nop 3

.LBB0_531:
	s_or_b64 exec, exec, s[0:1]
	v_add_f32_e32 v75, -1.0, v72
	v_mov_b32_e32 v86, v77
	v_pk_mul_f32 v[84:85], v[76:77], v[76:77]
	v_pk_mul_f32 v[86:87], v[86:87], v[74:75] op_sel:[0,1] op_sel_hi:[0,0]
	v_pk_fma_f32 v[88:89], v[76:77], v[74:75], v[86:87] op_sel_hi:[0,1,1]
	v_pk_add_f32 v[84:85], v[84:85], v[84:85] op_sel:[0,1] op_sel_hi:[0,1]
	v_div_scale_f32 v71, s[0:1], v85, v85, v89
	v_rcp_f32_e32 v73, v71
	v_pk_fma_f32 v[76:77], v[76:77], v[74:75], v[86:87] op_sel_hi:[0,1,1] neg_lo:[0,0,1] neg_hi:[0,0,1]
	s_waitcnt vmcnt(0) lgkmcnt(0)
	v_mul_f32_e32 v101, v93, v0
	v_mul_hi_i32 v0, v90, s78
	v_fma_f32 v75, -v71, v73, 1.0
	v_fmac_f32_e32 v73, v75, v73
	v_div_scale_f32 v75, vcc, v89, v85, v89
	v_mul_f32_e32 v77, v75, v73
	v_fma_f32 v81, -v71, v77, v75
	v_fmac_f32_e32 v77, v81, v73
	v_fma_f32 v71, -v71, v77, v75
	v_div_fmas_f32 v71, v71, v73, v77
	v_div_fixup_f32 v85, v71, v85, v89
	v_div_scale_f32 v71, s[0:1], v84, v84, v76
	v_rcp_f32_e32 v73, v71
	v_add_u32_e32 v0, v0, v90
	v_mul_f32_e32 v102, v93, v1
	v_lshrrev_b32_e32 v1, 31, v0
	v_fma_f32 v75, -v71, v73, 1.0
	v_fmac_f32_e32 v73, v75, v73
	v_div_scale_f32 v75, vcc, v76, v84, v76
	v_mul_f32_e32 v77, v75, v73
	v_fma_f32 v81, -v71, v77, v75
	v_fmac_f32_e32 v77, v81, v73
	v_fma_f32 v71, -v71, v77, v75
	v_div_fmas_f32 v71, v71, v73, v77
	v_div_fixup_f32 v84, v71, v84, v76
	v_pk_mul_f32 v[76:77], v[60:61], v[84:85] op_sel:[0,1] op_sel_hi:[0,0]
	v_pk_fma_f32 v[86:87], v[56:57], v[84:85], v[76:77] op_sel_hi:[0,1,1] neg_lo:[0,0,1] neg_hi:[0,0,1]
	v_pk_fma_f32 v[76:77], v[56:57], v[84:85], v[76:77] op_sel_hi:[0,1,1]
	v_pk_mul_f32 v[60:61], v[60:61], v[84:85] op_sel:[1,1] op_sel_hi:[1,0]
	v_mov_b32_e32 v77, v87
	v_pk_fma_f32 v[86:87], v[56:57], v[84:85], v[60:61] op_sel:[1,0,0] neg_lo:[0,0,1] neg_hi:[0,0,1]
	v_pk_fma_f32 v[56:57], v[56:57], v[84:85], v[60:61] op_sel:[1,0,0]
	v_pk_mul_f32 v[60:61], v[62:63], v[84:85] op_sel:[0,1] op_sel_hi:[0,0]
	v_mov_b32_e32 v57, v87
	v_pk_fma_f32 v[86:87], v[58:59], v[84:85], v[60:61] op_sel_hi:[0,1,1] neg_lo:[0,0,1] neg_hi:[0,0,1]
	v_pk_fma_f32 v[60:61], v[58:59], v[84:85], v[60:61] op_sel_hi:[0,1,1]
	v_mov_b32_e32 v58, v63
	v_pk_mul_f32 v[62:63], v[58:59], v[84:85] op_sel:[0,1] op_sel_hi:[0,0]
	v_mov_b32_e32 v58, v59
	v_mov_b32_e32 v61, v87
	v_pk_fma_f32 v[86:87], v[58:59], v[84:85], v[62:63] op_sel_hi:[0,1,1] neg_lo:[0,0,1] neg_hi:[0,0,1]
	v_pk_fma_f32 v[58:59], v[58:59], v[84:85], v[62:63] op_sel_hi:[0,1,1]
	v_pk_mul_f32 v[62:63], v[84:85], v[52:53] op_sel:[1,0] op_sel_hi:[0,0]
	v_mov_b32_e32 v59, v87
	v_pk_fma_f32 v[86:87], v[48:49], v[84:85], v[62:63] op_sel_hi:[0,1,1] neg_lo:[0,0,1] neg_hi:[0,0,1]
	v_pk_fma_f32 v[62:63], v[48:49], v[84:85], v[62:63] op_sel_hi:[0,1,1]
	v_pk_mul_f32 v[52:53], v[84:85], v[52:53] op_sel:[1,1] op_sel_hi:[0,1]
	v_mov_b32_e32 v63, v87
	v_pk_fma_f32 v[86:87], v[48:49], v[84:85], v[52:53] op_sel:[1,0,0] neg_lo:[0,0,1] neg_hi:[0,0,1]
	v_pk_fma_f32 v[48:49], v[48:49], v[84:85], v[52:53] op_sel:[1,0,0]
	v_pk_mul_f32 v[52:53], v[84:85], v[54:55] op_sel:[1,0] op_sel_hi:[0,0]
	v_mov_b32_e32 v49, v87
	v_pk_fma_f32 v[86:87], v[50:51], v[84:85], v[52:53] op_sel_hi:[0,1,1] neg_lo:[0,0,1] neg_hi:[0,0,1]
	v_pk_fma_f32 v[52:53], v[50:51], v[84:85], v[52:53] op_sel_hi:[0,1,1]
	v_mov_b32_e32 v50, v55
	v_pk_mul_f32 v[54:55], v[84:85], v[50:51] op_sel:[1,0] op_sel_hi:[0,0]
	v_mov_b32_e32 v50, v51
	v_mov_b32_e32 v53, v87
	v_pk_fma_f32 v[86:87], v[50:51], v[84:85], v[54:55] op_sel_hi:[0,1,1] neg_lo:[0,0,1] neg_hi:[0,0,1]
	v_pk_fma_f32 v[50:51], v[50:51], v[84:85], v[54:55] op_sel_hi:[0,1,1]
	v_pk_mul_f32 v[54:55], v[84:85], v[44:45] op_sel:[1,0] op_sel_hi:[0,0]
	v_mov_b32_e32 v51, v87
	v_pk_fma_f32 v[86:87], v[84:85], v[40:41], v[54:55] op_sel_hi:[1,0,1] neg_lo:[0,0,1] neg_hi:[0,0,1]
	v_pk_fma_f32 v[54:55], v[84:85], v[40:41], v[54:55] op_sel_hi:[1,0,1]
	v_pk_mul_f32 v[44:45], v[84:85], v[44:45] op_sel:[1,1] op_sel_hi:[0,1]
	v_mov_b32_e32 v55, v87
	v_pk_fma_f32 v[86:87], v[84:85], v[40:41], v[44:45] op_sel:[0,1,0] neg_lo:[0,0,1] neg_hi:[0,0,1]
	v_pk_fma_f32 v[40:41], v[84:85], v[40:41], v[44:45] op_sel:[0,1,0]
	v_pk_mul_f32 v[44:45], v[84:85], v[46:47] op_sel:[1,0] op_sel_hi:[0,0]
	v_mov_b32_e32 v41, v87
	v_pk_fma_f32 v[86:87], v[84:85], v[42:43], v[44:45] op_sel_hi:[1,0,1] neg_lo:[0,0,1] neg_hi:[0,0,1]
	v_pk_fma_f32 v[44:45], v[84:85], v[42:43], v[44:45] op_sel_hi:[1,0,1]
	v_mov_b32_e32 v42, v47
	v_pk_mul_f32 v[46:47], v[84:85], v[42:43] op_sel:[1,0] op_sel_hi:[0,0]
	v_mov_b32_e32 v42, v43
	v_mov_b32_e32 v45, v87
	v_pk_fma_f32 v[86:87], v[84:85], v[42:43], v[46:47] op_sel_hi:[1,0,1] neg_lo:[0,0,1] neg_hi:[0,0,1]
	v_pk_fma_f32 v[42:43], v[84:85], v[42:43], v[46:47] op_sel_hi:[1,0,1]
	v_pk_mul_f32 v[46:47], v[84:85], v[36:37] op_sel:[1,0] op_sel_hi:[0,0]
	v_mov_b32_e32 v43, v87
	v_pk_fma_f32 v[86:87], v[84:85], v[24:25], v[46:47] op_sel_hi:[1,0,1] neg_lo:[0,0,1] neg_hi:[0,0,1]
	v_pk_fma_f32 v[46:47], v[84:85], v[24:25], v[46:47] op_sel_hi:[1,0,1]
	v_pk_mul_f32 v[36:37], v[84:85], v[36:37] op_sel:[1,1] op_sel_hi:[0,1]
	v_ashrrev_i32_e32 v0, 9, v0
	v_mov_b32_e32 v47, v87
	v_pk_fma_f32 v[86:87], v[84:85], v[24:25], v[36:37] op_sel:[0,1,0] neg_lo:[0,0,1] neg_hi:[0,0,1]
	v_pk_fma_f32 v[24:25], v[84:85], v[24:25], v[36:37] op_sel:[0,1,0]
	v_pk_mul_f32 v[36:37], v[84:85], v[38:39] op_sel:[1,0] op_sel_hi:[0,0]
	v_add_u32_e32 v0, v0, v1
	v_mov_b32_e32 v25, v87
	v_pk_fma_f32 v[86:87], v[84:85], v[26:27], v[36:37] op_sel_hi:[1,0,1] neg_lo:[0,0,1] neg_hi:[0,0,1]
	v_pk_fma_f32 v[36:37], v[84:85], v[26:27], v[36:37] op_sel_hi:[1,0,1]
	v_mov_b32_e32 v26, v39
	v_ashrrev_i32_e32 v1, 31, v0
	v_ashrrev_i32_e32 v83, 31, v82
	v_pk_mul_f32 v[38:39], v[84:85], v[26:27] op_sel:[1,0] op_sel_hi:[0,0]
	v_mov_b32_e32 v26, v27
	v_mul_f32_e32 v103, v93, v2
	v_mul_f32_e32 v104, v93, v3
	v_lshlrev_b64 v[0:1], 11, v[0:1]
	v_lshlrev_b64 v[2:3], 6, v[82:83]
	v_mov_b32_e32 v37, v87
	v_pk_fma_f32 v[86:87], v[84:85], v[26:27], v[38:39] op_sel_hi:[1,0,1] neg_lo:[0,0,1] neg_hi:[0,0,1]
	v_pk_fma_f32 v[26:27], v[84:85], v[26:27], v[38:39] op_sel_hi:[1,0,1]
	v_mul_f32_e32 v38, v93, v8
	v_mul_f32_e32 v39, v93, v9
	v_lshl_add_u64 v[8:9], v[0:1], 0, v[2:3]
	v_mov_b64_e32 v[0:1], s[10:11]
	v_mad_u64_u32 v[0:1], s[0:1], v8, s80, v[0:1]
	v_ashrrev_i32_e32 v81, 31, v80
	v_mul_f32_e32 v84, v93, v10
	v_mul_f32_e32 v85, v93, v11
	v_mad_i32_i24 v1, v9, s80, v1
	v_lshlrev_b64 v[10:11], 1, v[80:81]
	v_lshl_add_u64 v[0:1], v[0:1], 0, v[10:11]
	v_mov_b32_e32 v71, v145
	v_mov_b32_e32 v27, v87
	v_mul_f32_e32 v86, v93, v4
	v_mul_f32_e32 v87, v93, v5
	v_lshl_add_u64 v[4:5], v[0:1], 0, v[70:71]
	v_mul_f32_e32 v88, v93, v6
	v_mul_f32_e32 v89, v93, v7
	s_waitcnt vmcnt(0)
	v_mov_b64_e32 v[0:1], v[140:141]
	v_mov_b64_e32 v[2:3], v[142:143]
	v_mov_b64_e32 v[4:5], v[136:137]
	v_mov_b64_e32 v[6:7], v[138:139]
	ds_write_b128 v98, v[4:7]
	ds_write_b128 v98, v[0:3] offset:16
	v_lshlrev_b32_e32 v132, 1, v97
	v_add_u32_e32 v132, 0x14800, v132
	v_lshl_add_u32 v134, v91, 6, v132
	v_lshlrev_b32_e32 v146, 16, v4
	v_and_b32_e32 v147, 0xffff0000, v4
	v_lshlrev_b32_e32 v148, 16, v5
	v_and_b32_e32 v149, 0xffff0000, v5
	v_lshlrev_b32_e32 v150, 16, v6
	v_and_b32_e32 v151, 0xffff0000, v6
	v_lshlrev_b32_e32 v152, 16, v7
	v_and_b32_e32 v153, 0xffff0000, v7
	v_lshlrev_b32_e32 v154, 16, v0
	v_and_b32_e32 v155, 0xffff0000, v0
	v_lshlrev_b32_e32 v156, 16, v1
	v_and_b32_e32 v157, 0xffff0000, v1
	v_lshlrev_b32_e32 v158, 16, v2
	v_and_b32_e32 v159, 0xffff0000, v2
	v_lshlrev_b32_e32 v160, 16, v3
	v_and_b32_e32 v161, 0xffff0000, v3
	ds_write_b128 v134, v[146:149]
	ds_write_b128 v134, v[150:153] offset:16
	ds_write_b128 v134, v[154:157] offset:32
	ds_write_b128 v134, v[158:161] offset:48
	s_waitcnt lgkmcnt(0)
	v_mul_f32_e32 v32, v93, v32
	v_mul_f32_e32 v33, v93, v33
	v_mul_f32_e32 v34, v93, v34
	v_mul_f32_e32 v35, v93, v35
	v_mul_f32_e32 v28, v93, v28
	v_mul_f32_e32 v29, v93, v29
	v_mul_f32_e32 v30, v93, v30
	v_mul_f32_e32 v31, v93, v31
	v_mul_f32_e32 v20, v93, v20
	v_mul_f32_e32 v21, v93, v21
	v_mul_f32_e32 v22, v93, v22
	v_mul_f32_e32 v23, v93, v23
	v_mul_f32_e32 v16, v93, v16
	v_mul_f32_e32 v17, v93, v17
	v_mul_f32_e32 v18, v93, v18
	v_mul_f32_e32 v19, v93, v19
	v_mul_f32_e32 v12, v93, v12
	v_mul_f32_e32 v13, v93, v13
	v_mul_f32_e32 v14, v93, v14
	v_mul_f32_e32 v15, v93, v15
	v_xor_b32_e32 v75, 0x80000000, v74
	v_lshl_add_u64 v[0:1], v[80:81], 2, v[66:67]
	v_lshl_add_u64 v[2:3], v[68:69], 0, v[10:11]
	v_mov_b32_e32 v73, v72
	s_mov_b32 s0, 0
	v_mov_b32_e32 v6, v97
